# agg gather: odd-sized batch first, then an 8-deep ring: every slot is refilled right after it is consumed for all degrees above 8
# baseline (speedup 1.0000x reference)
.Lagg_inner:
	s_sub_u32 s16, s14, s15
	s_and_b32 s16, s16, 7
	s_cmp_eq_u32 s16, 0
	s_cselect_b32 s16, 8, s16
	s_cmp_ge_u32 s16, 8
	s_cbranch_scc1 .Lagg_ld7
	s_cmp_ge_u32 s16, 7
	s_cbranch_scc1 .Lagg_ld6
	s_cmp_ge_u32 s16, 6
	s_cbranch_scc1 .Lagg_ld5
	s_cmp_ge_u32 s16, 5
	s_cbranch_scc1 .Lagg_ld4
	s_cmp_ge_u32 s16, 4
	s_cbranch_scc1 .Lagg_ld3
	s_cmp_ge_u32 s16, 3
	s_cbranch_scc1 .Lagg_ld2
	s_cmp_ge_u32 s16, 2
	s_cbranch_scc1 .Lagg_ld1
	s_branch .Lagg_ld0

.Lagg_chk:
	s_sub_u32 s17, s14, s15
	s_cmp_le_u32 s17, s16
	s_cbranch_scc1 .Lagg_cons
	s_mov_b32 s30, s16
	s_add_u32 s15, s15, s16
	s_sub_u32 s15, s15, 8
	s_branch .Lagg_pipe
.Lagg_cons:
	s_cmp_ge_u32 s16, 8
	s_cbranch_scc1 .Lagg_ac7
	s_cmp_ge_u32 s16, 7
	s_cbranch_scc1 .Lagg_ac6
	s_cmp_ge_u32 s16, 6
	s_cbranch_scc1 .Lagg_ac5
	s_cmp_ge_u32 s16, 5
	s_cbranch_scc1 .Lagg_ac4
	s_cmp_ge_u32 s16, 4
	s_cbranch_scc1 .Lagg_ac3
	s_cmp_ge_u32 s16, 3
	s_cbranch_scc1 .Lagg_ac2
	s_cmp_ge_u32 s16, 2
	s_cbranch_scc1 .Lagg_ac1
	s_branch .Lagg_ac0

.Lagg_pipe:
	s_cmp_le_u32 s30, 7
	s_cbranch_scc1 .Lagg_pf7
	s_waitcnt vmcnt(14)
	v_cvt_f32_i32_sdwa v2, sext(v54) dst_sel:DWORD dst_unused:UNUSED_PAD src0_sel:BYTE_0
	v_cvt_f32_i32_sdwa v3, sext(v54) dst_sel:DWORD dst_unused:UNUSED_PAD src0_sel:BYTE_1
	v_cvt_f32_i32_sdwa v22, sext(v54) dst_sel:DWORD dst_unused:UNUSED_PAD src0_sel:BYTE_2
	v_cvt_f32_i32_sdwa v23, sext(v54) dst_sel:DWORD dst_unused:UNUSED_PAD src0_sel:BYTE_3
	v_cvt_f32_i32_sdwa v26, sext(v55) dst_sel:DWORD dst_unused:UNUSED_PAD src0_sel:BYTE_0
	v_cvt_f32_i32_sdwa v27, sext(v55) dst_sel:DWORD dst_unused:UNUSED_PAD src0_sel:BYTE_1
	v_cvt_f32_i32_sdwa v28, sext(v55) dst_sel:DWORD dst_unused:UNUSED_PAD src0_sel:BYTE_2
	v_cvt_f32_i32_sdwa v29, sext(v55) dst_sel:DWORD dst_unused:UNUSED_PAD src0_sel:BYTE_3
	v_pk_fma_f32 v[16:17], v[38:39], v[2:3], v[16:17] op_sel:[1,0,0] op_sel_hi:[1,1,1]
	v_pk_fma_f32 v[14:15], v[38:39], v[22:23], v[14:15] op_sel:[1,0,0] op_sel_hi:[1,1,1]
	v_pk_fma_f32 v[12:13], v[38:39], v[26:27], v[12:13] op_sel:[1,0,0] op_sel_hi:[1,1,1]
	v_pk_fma_f32 v[10:11], v[38:39], v[28:29], v[10:11] op_sel:[1,0,0] op_sel_hi:[1,1,1]
.Lagg_pf7:
	s_add_u32 s17, s15, 15
	v_readlane_b32 s28, v6, s17
	s_mul_i32 s29, s28, 0x220
	s_add_u32 s54, s26, s29
	s_addc_u32 s55, s27, 0
	global_load_dwordx2 v[54:55], v8, s[54:55]
	global_load_dword v39, v20, s[54:55] offset:512
	s_cmp_le_u32 s30, 6
	s_cbranch_scc1 .Lagg_pf6
	s_waitcnt vmcnt(14)
	v_cvt_f32_i32_sdwa v2, sext(v52) dst_sel:DWORD dst_unused:UNUSED_PAD src0_sel:BYTE_0
	v_cvt_f32_i32_sdwa v3, sext(v52) dst_sel:DWORD dst_unused:UNUSED_PAD src0_sel:BYTE_1
	v_cvt_f32_i32_sdwa v22, sext(v52) dst_sel:DWORD dst_unused:UNUSED_PAD src0_sel:BYTE_2
	v_cvt_f32_i32_sdwa v23, sext(v52) dst_sel:DWORD dst_unused:UNUSED_PAD src0_sel:BYTE_3
	v_cvt_f32_i32_sdwa v26, sext(v53) dst_sel:DWORD dst_unused:UNUSED_PAD src0_sel:BYTE_0
	v_cvt_f32_i32_sdwa v27, sext(v53) dst_sel:DWORD dst_unused:UNUSED_PAD src0_sel:BYTE_1
	v_cvt_f32_i32_sdwa v28, sext(v53) dst_sel:DWORD dst_unused:UNUSED_PAD src0_sel:BYTE_2
	v_cvt_f32_i32_sdwa v29, sext(v53) dst_sel:DWORD dst_unused:UNUSED_PAD src0_sel:BYTE_3
	v_pk_fma_f32 v[16:17], v[38:39], v[2:3], v[16:17] op_sel_hi:[0,1,1]
	v_pk_fma_f32 v[14:15], v[38:39], v[22:23], v[14:15] op_sel_hi:[0,1,1]
	v_pk_fma_f32 v[12:13], v[38:39], v[26:27], v[12:13] op_sel_hi:[0,1,1]
	v_pk_fma_f32 v[10:11], v[38:39], v[28:29], v[10:11] op_sel_hi:[0,1,1]
.Lagg_pf6:
	s_add_u32 s17, s15, 14
	v_readlane_b32 s28, v6, s17
	s_mul_i32 s29, s28, 0x220
	s_add_u32 s52, s26, s29
	s_addc_u32 s53, s27, 0
	global_load_dwordx2 v[52:53], v8, s[52:53]
	global_load_dword v38, v20, s[52:53] offset:512
	s_cmp_le_u32 s30, 5
	s_cbranch_scc1 .Lagg_pf5
	s_waitcnt vmcnt(14)
	v_cvt_f32_i32_sdwa v2, sext(v50) dst_sel:DWORD dst_unused:UNUSED_PAD src0_sel:BYTE_0
	v_cvt_f32_i32_sdwa v3, sext(v50) dst_sel:DWORD dst_unused:UNUSED_PAD src0_sel:BYTE_1
	v_cvt_f32_i32_sdwa v22, sext(v50) dst_sel:DWORD dst_unused:UNUSED_PAD src0_sel:BYTE_2
	v_cvt_f32_i32_sdwa v23, sext(v50) dst_sel:DWORD dst_unused:UNUSED_PAD src0_sel:BYTE_3
	v_cvt_f32_i32_sdwa v26, sext(v51) dst_sel:DWORD dst_unused:UNUSED_PAD src0_sel:BYTE_0
	v_cvt_f32_i32_sdwa v27, sext(v51) dst_sel:DWORD dst_unused:UNUSED_PAD src0_sel:BYTE_1
	v_cvt_f32_i32_sdwa v28, sext(v51) dst_sel:DWORD dst_unused:UNUSED_PAD src0_sel:BYTE_2
	v_cvt_f32_i32_sdwa v29, sext(v51) dst_sel:DWORD dst_unused:UNUSED_PAD src0_sel:BYTE_3
	v_pk_fma_f32 v[16:17], v[36:37], v[2:3], v[16:17] op_sel:[1,0,0] op_sel_hi:[1,1,1]
	v_pk_fma_f32 v[14:15], v[36:37], v[22:23], v[14:15] op_sel:[1,0,0] op_sel_hi:[1,1,1]
	v_pk_fma_f32 v[12:13], v[36:37], v[26:27], v[12:13] op_sel:[1,0,0] op_sel_hi:[1,1,1]
	v_pk_fma_f32 v[10:11], v[36:37], v[28:29], v[10:11] op_sel:[1,0,0] op_sel_hi:[1,1,1]
.Lagg_pf5:
	s_add_u32 s17, s15, 13
	v_readlane_b32 s28, v6, s17
	s_mul_i32 s29, s28, 0x220
	s_add_u32 s50, s26, s29
	s_addc_u32 s51, s27, 0
	global_load_dwordx2 v[50:51], v8, s[50:51]
	global_load_dword v37, v20, s[50:51] offset:512
	s_cmp_le_u32 s30, 4
	s_cbranch_scc1 .Lagg_pf4
	s_waitcnt vmcnt(14)
	v_cvt_f32_i32_sdwa v2, sext(v48) dst_sel:DWORD dst_unused:UNUSED_PAD src0_sel:BYTE_0
	v_cvt_f32_i32_sdwa v3, sext(v48) dst_sel:DWORD dst_unused:UNUSED_PAD src0_sel:BYTE_1
	v_cvt_f32_i32_sdwa v22, sext(v48) dst_sel:DWORD dst_unused:UNUSED_PAD src0_sel:BYTE_2
	v_cvt_f32_i32_sdwa v23, sext(v48) dst_sel:DWORD dst_unused:UNUSED_PAD src0_sel:BYTE_3
	v_cvt_f32_i32_sdwa v26, sext(v49) dst_sel:DWORD dst_unused:UNUSED_PAD src0_sel:BYTE_0
	v_cvt_f32_i32_sdwa v27, sext(v49) dst_sel:DWORD dst_unused:UNUSED_PAD src0_sel:BYTE_1
	v_cvt_f32_i32_sdwa v28, sext(v49) dst_sel:DWORD dst_unused:UNUSED_PAD src0_sel:BYTE_2
	v_cvt_f32_i32_sdwa v29, sext(v49) dst_sel:DWORD dst_unused:UNUSED_PAD src0_sel:BYTE_3
	v_pk_fma_f32 v[16:17], v[36:37], v[2:3], v[16:17] op_sel_hi:[0,1,1]
	v_pk_fma_f32 v[14:15], v[36:37], v[22:23], v[14:15] op_sel_hi:[0,1,1]
	v_pk_fma_f32 v[12:13], v[36:37], v[26:27], v[12:13] op_sel_hi:[0,1,1]
	v_pk_fma_f32 v[10:11], v[36:37], v[28:29], v[10:11] op_sel_hi:[0,1,1]
.Lagg_pf4:
	s_add_u32 s17, s15, 12
	v_readlane_b32 s28, v6, s17
	s_mul_i32 s29, s28, 0x220
	s_add_u32 s48, s26, s29
	s_addc_u32 s49, s27, 0
	global_load_dwordx2 v[48:49], v8, s[48:49]
	global_load_dword v36, v20, s[48:49] offset:512
	s_cmp_le_u32 s30, 3
	s_cbranch_scc1 .Lagg_pf3
	s_waitcnt vmcnt(14)
	v_cvt_f32_i32_sdwa v2, sext(v46) dst_sel:DWORD dst_unused:UNUSED_PAD src0_sel:BYTE_0
	v_cvt_f32_i32_sdwa v3, sext(v46) dst_sel:DWORD dst_unused:UNUSED_PAD src0_sel:BYTE_1
	v_cvt_f32_i32_sdwa v22, sext(v46) dst_sel:DWORD dst_unused:UNUSED_PAD src0_sel:BYTE_2
	v_cvt_f32_i32_sdwa v23, sext(v46) dst_sel:DWORD dst_unused:UNUSED_PAD src0_sel:BYTE_3
	v_cvt_f32_i32_sdwa v26, sext(v47) dst_sel:DWORD dst_unused:UNUSED_PAD src0_sel:BYTE_0
	v_cvt_f32_i32_sdwa v27, sext(v47) dst_sel:DWORD dst_unused:UNUSED_PAD src0_sel:BYTE_1
	v_cvt_f32_i32_sdwa v28, sext(v47) dst_sel:DWORD dst_unused:UNUSED_PAD src0_sel:BYTE_2
	v_cvt_f32_i32_sdwa v29, sext(v47) dst_sel:DWORD dst_unused:UNUSED_PAD src0_sel:BYTE_3
	v_pk_fma_f32 v[16:17], v[34:35], v[2:3], v[16:17] op_sel:[1,0,0] op_sel_hi:[1,1,1]
	v_pk_fma_f32 v[14:15], v[34:35], v[22:23], v[14:15] op_sel:[1,0,0] op_sel_hi:[1,1,1]
	v_pk_fma_f32 v[12:13], v[34:35], v[26:27], v[12:13] op_sel:[1,0,0] op_sel_hi:[1,1,1]
	v_pk_fma_f32 v[10:11], v[34:35], v[28:29], v[10:11] op_sel:[1,0,0] op_sel_hi:[1,1,1]
.Lagg_pf3:
	s_add_u32 s17, s15, 11
	v_readlane_b32 s28, v6, s17
	s_mul_i32 s29, s28, 0x220
	s_add_u32 s46, s26, s29
	s_addc_u32 s47, s27, 0
	global_load_dwordx2 v[46:47], v8, s[46:47]
	global_load_dword v35, v20, s[46:47] offset:512
	s_cmp_le_u32 s30, 2
	s_cbranch_scc1 .Lagg_pf2
	s_waitcnt vmcnt(14)
	v_cvt_f32_i32_sdwa v2, sext(v44) dst_sel:DWORD dst_unused:UNUSED_PAD src0_sel:BYTE_0
	v_cvt_f32_i32_sdwa v3, sext(v44) dst_sel:DWORD dst_unused:UNUSED_PAD src0_sel:BYTE_1
	v_cvt_f32_i32_sdwa v22, sext(v44) dst_sel:DWORD dst_unused:UNUSED_PAD src0_sel:BYTE_2
	v_cvt_f32_i32_sdwa v23, sext(v44) dst_sel:DWORD dst_unused:UNUSED_PAD src0_sel:BYTE_3
	v_cvt_f32_i32_sdwa v26, sext(v45) dst_sel:DWORD dst_unused:UNUSED_PAD src0_sel:BYTE_0
	v_cvt_f32_i32_sdwa v27, sext(v45) dst_sel:DWORD dst_unused:UNUSED_PAD src0_sel:BYTE_1
	v_cvt_f32_i32_sdwa v28, sext(v45) dst_sel:DWORD dst_unused:UNUSED_PAD src0_sel:BYTE_2
	v_cvt_f32_i32_sdwa v29, sext(v45) dst_sel:DWORD dst_unused:UNUSED_PAD src0_sel:BYTE_3
	v_pk_fma_f32 v[16:17], v[34:35], v[2:3], v[16:17] op_sel_hi:[0,1,1]
	v_pk_fma_f32 v[14:15], v[34:35], v[22:23], v[14:15] op_sel_hi:[0,1,1]
	v_pk_fma_f32 v[12:13], v[34:35], v[26:27], v[12:13] op_sel_hi:[0,1,1]
	v_pk_fma_f32 v[10:11], v[34:35], v[28:29], v[10:11] op_sel_hi:[0,1,1]
.Lagg_pf2:
	s_add_u32 s17, s15, 10
	v_readlane_b32 s28, v6, s17
	s_mul_i32 s29, s28, 0x220
	s_add_u32 s44, s26, s29
	s_addc_u32 s45, s27, 0
	global_load_dwordx2 v[44:45], v8, s[44:45]
	global_load_dword v34, v20, s[44:45] offset:512
	s_cmp_le_u32 s30, 1
	s_cbranch_scc1 .Lagg_pf1
	s_waitcnt vmcnt(14)
	v_cvt_f32_i32_sdwa v2, sext(v42) dst_sel:DWORD dst_unused:UNUSED_PAD src0_sel:BYTE_0
	v_cvt_f32_i32_sdwa v3, sext(v42) dst_sel:DWORD dst_unused:UNUSED_PAD src0_sel:BYTE_1
	v_cvt_f32_i32_sdwa v22, sext(v42) dst_sel:DWORD dst_unused:UNUSED_PAD src0_sel:BYTE_2
	v_cvt_f32_i32_sdwa v23, sext(v42) dst_sel:DWORD dst_unused:UNUSED_PAD src0_sel:BYTE_3
	v_cvt_f32_i32_sdwa v26, sext(v43) dst_sel:DWORD dst_unused:UNUSED_PAD src0_sel:BYTE_0
	v_cvt_f32_i32_sdwa v27, sext(v43) dst_sel:DWORD dst_unused:UNUSED_PAD src0_sel:BYTE_1
	v_cvt_f32_i32_sdwa v28, sext(v43) dst_sel:DWORD dst_unused:UNUSED_PAD src0_sel:BYTE_2
	v_cvt_f32_i32_sdwa v29, sext(v43) dst_sel:DWORD dst_unused:UNUSED_PAD src0_sel:BYTE_3
	v_pk_fma_f32 v[16:17], v[32:33], v[2:3], v[16:17] op_sel:[1,0,0] op_sel_hi:[1,1,1]
	v_pk_fma_f32 v[14:15], v[32:33], v[22:23], v[14:15] op_sel:[1,0,0] op_sel_hi:[1,1,1]
	v_pk_fma_f32 v[12:13], v[32:33], v[26:27], v[12:13] op_sel:[1,0,0] op_sel_hi:[1,1,1]
	v_pk_fma_f32 v[10:11], v[32:33], v[28:29], v[10:11] op_sel:[1,0,0] op_sel_hi:[1,1,1]
.Lagg_pf1:
	s_add_u32 s17, s15, 9
	v_readlane_b32 s28, v6, s17
	s_mul_i32 s29, s28, 0x220
	s_add_u32 s42, s26, s29
	s_addc_u32 s43, s27, 0
	global_load_dwordx2 v[42:43], v8, s[42:43]
	global_load_dword v33, v20, s[42:43] offset:512
	s_cmp_le_u32 s30, 0
	s_cbranch_scc1 .Lagg_pf0
	s_waitcnt vmcnt(14)
	v_cvt_f32_i32_sdwa v2, sext(v40) dst_sel:DWORD dst_unused:UNUSED_PAD src0_sel:BYTE_0
	v_cvt_f32_i32_sdwa v3, sext(v40) dst_sel:DWORD dst_unused:UNUSED_PAD src0_sel:BYTE_1
	v_cvt_f32_i32_sdwa v22, sext(v40) dst_sel:DWORD dst_unused:UNUSED_PAD src0_sel:BYTE_2
	v_cvt_f32_i32_sdwa v23, sext(v40) dst_sel:DWORD dst_unused:UNUSED_PAD src0_sel:BYTE_3
	v_cvt_f32_i32_sdwa v26, sext(v41) dst_sel:DWORD dst_unused:UNUSED_PAD src0_sel:BYTE_0
	v_cvt_f32_i32_sdwa v27, sext(v41) dst_sel:DWORD dst_unused:UNUSED_PAD src0_sel:BYTE_1
	v_cvt_f32_i32_sdwa v28, sext(v41) dst_sel:DWORD dst_unused:UNUSED_PAD src0_sel:BYTE_2
	v_cvt_f32_i32_sdwa v29, sext(v41) dst_sel:DWORD dst_unused:UNUSED_PAD src0_sel:BYTE_3
	v_pk_fma_f32 v[16:17], v[32:33], v[2:3], v[16:17] op_sel_hi:[0,1,1]
	v_pk_fma_f32 v[14:15], v[32:33], v[22:23], v[14:15] op_sel_hi:[0,1,1]
	v_pk_fma_f32 v[12:13], v[32:33], v[26:27], v[12:13] op_sel_hi:[0,1,1]
	v_pk_fma_f32 v[10:11], v[32:33], v[28:29], v[10:11] op_sel_hi:[0,1,1]
.Lagg_pf0:
	s_add_u32 s17, s15, 8
	v_readlane_b32 s28, v6, s17
	s_mul_i32 s29, s28, 0x220
	s_add_u32 s40, s26, s29
	s_addc_u32 s41, s27, 0
	global_load_dwordx2 v[40:41], v8, s[40:41]
	global_load_dword v32, v20, s[40:41] offset:512
	s_add_u32 s15, s15, 8
	s_mov_b32 s16, 8
	s_branch .Lagg_chk
